# speedup vs baseline: 1.0068x; 1.0068x over previous
.LBB15_10:
	s_or_b64 exec, exec, s[4:5]
	v_bfe_u32 v156, v0, 6, 1
	v_lshrrev_b32_e32 v4, 1, v0
	s_load_dwordx2 s[8:9], s[0:1], 0x28
	v_and_b32_e32 v166, 31, v0
	v_lshrrev_b32_e32 v3, 5, v0
	v_lshlrev_b32_e32 v161, 6, v156
	v_and_b32_e32 v167, 0xc0, v4
	v_bfe_u32 v4, v0, 2, 2
	v_bitop3_b32 v169, v3, v4, 1 bitop3:0x6c
	v_or_b32_e32 v3, v166, v161
	v_bfe_u32 v159, v0, 5, 1
	v_lshlrev_b32_e32 v6, 2, v3
	v_mov_b32_e32 v3, 0
	v_bitop3_b32 v165, v159, v4, 2 bitop3:0x36
	v_lshl_add_u64 v[4:5], s[6:7], 0, v[2:3]
	s_mov_b64 s[0:1], 0x6000
	v_lshlrev_b32_e32 v2, 5, v0
	v_or_b32_e32 v160, 2, v159
	v_lshrrev_b32_e32 v158, 2, v0
	v_lshl_add_u64 v[150:151], v[4:5], 0, s[0:1]
	v_or_b32_e32 v170, v167, v166
	v_lshlrev_b32_e32 v171, 6, v166
	v_and_b32_e32 v172, 0x3000, v2
	s_movk_i32 s16, 0x200
	s_mov_b32 s17, 0
	v_lshlrev_b32_e32 v168, 4, v6
	s_mov_b32 s18, 0
	s_mov_b32 s19, 0
	v_mov_b32_e32 v2, 0
	v_mov_b32_e32 v4, v3
	v_mov_b32_e32 v5, v3
	v_mov_b32_e32 v6, v3
	v_mov_b32_e32 v7, v3
	v_mov_b32_e32 v8, v3
	v_mov_b32_e32 v9, v3
	v_mov_b32_e32 v10, v3
	v_mov_b32_e32 v11, v3
	v_mov_b32_e32 v12, v3
	v_mov_b32_e32 v13, v3
	v_mov_b32_e32 v14, v3
	v_mov_b32_e32 v15, v3
	v_mov_b32_e32 v16, v3
	v_mov_b32_e32 v17, v3
	v_mov_b32_e32 v18, 0
	v_mov_b32_e32 v19, v3
	v_mov_b32_e32 v20, v3
	v_mov_b32_e32 v21, v3
	v_mov_b32_e32 v22, v3
	v_mov_b32_e32 v23, v3
	v_mov_b32_e32 v24, v3
	v_mov_b32_e32 v25, v3
	v_mov_b32_e32 v26, v3
	v_mov_b32_e32 v27, v3
	v_mov_b32_e32 v28, v3
	v_mov_b32_e32 v29, v3
	v_mov_b32_e32 v30, v3
	v_mov_b32_e32 v31, v3
	v_mov_b32_e32 v32, v3
	v_mov_b32_e32 v33, v3
	v_mov_b32_e32 v50, 0
	v_mov_b32_e32 v51, v3
	v_mov_b32_e32 v52, v3
	v_mov_b32_e32 v53, v3
	v_mov_b32_e32 v54, v3
	v_mov_b32_e32 v55, v3
	v_mov_b32_e32 v56, v3
	v_mov_b32_e32 v57, v3
	v_mov_b32_e32 v58, v3
	v_mov_b32_e32 v59, v3
	v_mov_b32_e32 v60, v3
	v_mov_b32_e32 v61, v3
	v_mov_b32_e32 v62, v3
	v_mov_b32_e32 v63, v3
	v_mov_b32_e32 v64, v3
	v_mov_b32_e32 v65, v3
	v_mov_b32_e32 v82, 0
	v_mov_b32_e32 v83, v3
	v_mov_b32_e32 v84, v3
	v_mov_b32_e32 v85, v3
	v_mov_b32_e32 v86, v3
	v_mov_b32_e32 v87, v3
	v_mov_b32_e32 v88, v3
	v_mov_b32_e32 v89, v3
	v_mov_b32_e32 v90, v3
	v_mov_b32_e32 v91, v3
	v_mov_b32_e32 v92, v3
	v_mov_b32_e32 v93, v3
	v_mov_b32_e32 v94, v3
	v_mov_b32_e32 v95, v3
	v_mov_b32_e32 v96, v3
	v_mov_b32_e32 v97, v3
	v_mov_b32_e32 v34, 0
	v_mov_b32_e32 v35, v3
	v_mov_b32_e32 v36, v3
	v_mov_b32_e32 v37, v3
	v_mov_b32_e32 v38, v3
	v_mov_b32_e32 v39, v3
	v_mov_b32_e32 v40, v3
	v_mov_b32_e32 v41, v3
	v_mov_b32_e32 v42, v3
	v_mov_b32_e32 v43, v3
	v_mov_b32_e32 v44, v3
	v_mov_b32_e32 v45, v3
	v_mov_b32_e32 v46, v3
	v_mov_b32_e32 v47, v3
	v_mov_b32_e32 v48, v3
	v_mov_b32_e32 v49, v3
	v_mov_b32_e32 v66, 0
	v_mov_b32_e32 v67, v3
	v_mov_b32_e32 v68, v3
	v_mov_b32_e32 v69, v3
	v_mov_b32_e32 v70, v3
	v_mov_b32_e32 v71, v3
	v_mov_b32_e32 v72, v3
	v_mov_b32_e32 v73, v3
	v_mov_b32_e32 v74, v3
	v_mov_b32_e32 v75, v3
	v_mov_b32_e32 v76, v3
	v_mov_b32_e32 v77, v3
	v_mov_b32_e32 v78, v3
	v_mov_b32_e32 v79, v3
	v_mov_b32_e32 v80, v3
	v_mov_b32_e32 v81, v3
	v_mov_b32_e32 v98, 0
	v_mov_b32_e32 v99, v3
	v_mov_b32_e32 v100, v3
	v_mov_b32_e32 v101, v3
	v_mov_b32_e32 v102, v3
	v_mov_b32_e32 v103, v3
	v_mov_b32_e32 v104, v3
	v_mov_b32_e32 v105, v3
	v_mov_b32_e32 v106, v3
	v_mov_b32_e32 v107, v3
	v_mov_b32_e32 v108, v3
	v_mov_b32_e32 v109, v3
	v_mov_b32_e32 v110, v3
	v_mov_b32_e32 v111, v3
	v_mov_b32_e32 v112, v3
	v_mov_b32_e32 v113, v3
	v_mov_b32_e32 v114, 0
	v_mov_b32_e32 v115, v3
	v_mov_b32_e32 v116, v3
	v_mov_b32_e32 v117, v3
	v_mov_b32_e32 v118, v3
	v_mov_b32_e32 v119, v3
	v_mov_b32_e32 v120, v3
	v_mov_b32_e32 v121, v3
	v_mov_b32_e32 v122, v3
	v_mov_b32_e32 v123, v3
	v_mov_b32_e32 v124, v3
	v_mov_b32_e32 v125, v3
	v_mov_b32_e32 v126, v3
	v_mov_b32_e32 v127, v3
	v_mov_b32_e32 v128, v3
	v_mov_b32_e32 v129, v3
	s_waitcnt lgkmcnt(0)
	v_mov_b32_e32 v174, 0
	v_mov_b32_e32 v175, 0
	v_mov_b32_e32 v176, 0
	v_mov_b32_e32 v177, 0
	v_mov_b32_e32 v178, 0
	v_mov_b32_e32 v179, 0
	v_mov_b32_e32 v180, 0
	v_mov_b32_e32 v181, 0
	v_mov_b32_e32 v194, 0
	v_mov_b32_e32 v195, 0
	v_mov_b32_e32 v196, 0
	v_mov_b32_e32 v197, 0
	v_mov_b32_e32 v234, 0
	v_mov_b32_e32 v235, 0
	v_mov_b32_e32 v236, 0
	v_mov_b32_e32 v237, 0
	v_mov_b32_e32 v238, 0
	v_mov_b32_e32 v239, 0
	v_mov_b32_e32 v240, 0
	v_mov_b32_e32 v241, 0
	v_mov_b32_e32 v242, 0
	v_mov_b32_e32 v243, 0
	v_mov_b32_e32 v244, 0
	v_mov_b32_e32 v245, 0
	v_mov_b32_e32 v246, 0
	v_mov_b32_e32 v247, 0
	v_mov_b32_e32 v248, 0
	v_mov_b32_e32 v249, 0
	v_mov_b32_e32 v250, 0
	v_mov_b32_e32 v251, 0
	v_mov_b32_e32 v252, 0
	v_mov_b32_e32 v253, 0
	v_bfe_u32 v254, v0, 4, 2
	v_and_b32_e32 v255, 3, v0
	v_xor_b32_e32 v254, v254, v255
	v_sub_u32_e32 v254, v254, v255
	v_lshlrev_b32_e32 v254, 4, v254
	v_ashrrev_i32_e32 v255, 31, v254
	v_readfirstlane_b32 s25, v0
	s_lshl_b32 s25, s25, 4
	s_add_i32 s25, s25, 0x13700
	s_mov_b64 s[36:37], 0x2000
	s_barrier
	s_branch .LBB15_13

.LBB15_13:
	s_add_i32 s24, s19, 1
	s_and_b32 s24, s24, 1
	s_mul_i32 s24, s24, 0x6000
	s_add_i32 s24, s24, s25
	v_lshl_add_u64 v[130:131], v[150:151], 0, v[254:255]
	s_mov_b32 m0, s24
	v_mfma_f32_32x32x16_f16 v[82:97], v[178:181], v[194:197], v[82:97]
	global_load_lds_dwordx4 v[130:131], off
	v_lshl_add_u64 v[132:133], v[130:131], 0, s[36:37]
	s_add_i32 s24, s24, 0x2000
	s_mov_b32 m0, s24
	v_mfma_f32_32x32x16_f16 v[114:129], v[178:181], v[234:237], v[114:129]
	global_load_lds_dwordx4 v[132:133], off
	v_lshl_add_u64 v[132:133], v[132:133], 0, s[36:37]
	s_add_i32 s24, s24, 0x2000
	s_mov_b32 m0, s24
	v_mfma_f32_32x32x16_f16 v[114:129], v[246:249], v[194:197], v[114:129]
	global_load_lds_dwordx4 v[132:133], off
	s_mul_hi_u32 s4, s19, 0xaaaaaaab
	s_lshr_b32 s23, s4, 1
	s_mul_i32 s4, s23, 0x9ba
	s_sub_i32 s20, s16, s4
	s_sub_i32 s7, s17, s4
	v_mfma_f32_32x32x16_f16 v[50:65], v[178:181], v[238:241], v[50:65]
	s_mul_i32 s4, s19, 0xab
	s_mul_i32 s5, s23, 0x8880
	s_bfe_u32 s22, s4, 0x70009
	s_add_i32 s6, s5, 0x5b00
	s_add_i32 s22, s22, 1
	v_mfma_f32_32x32x16_f16 v[98:113], v[178:181], v[242:245], v[98:113]
	s_cmp_lt_u32 s19, 21
	s_cselect_b64 s[4:5], -1, 0
	s_add_i32 s12, s7, 0x33e
	s_cmp_lg_u32 s6, s18
	s_cselect_b32 s21, s12, 0x9b8
	v_mfma_f32_32x32x16_f16 v[98:113], v[246:249], v[238:241], v[98:113]
	v_add_u32_e32 v152, s7, v0
	s_cmp_gt_u32 s19, 20
	v_mov_b32_e32 v141, 0
	v_cmp_gt_i32_e32 vcc, s21, v152
	v_mov_b32_e32 v140, 0
	v_mfma_f32_32x32x16_f16 v[18:33], v[174:177], v[194:197], v[18:33]
	v_mov_b32_e32 v139, 0
	v_mov_b32_e32 v138, 0
	v_mov_b32_e32 v137, 0
	v_mov_b32_e32 v136, 0
	v_mov_b32_e32 v135, 0
	v_mfma_f32_32x32x16_f16 v[66:81], v[174:177], v[234:237], v[66:81]
	v_mov_b32_e32 v134, 0
	s_cbranch_scc1 .LBB15_21
	s_mul_i32 s6, s22, 0x206000
	s_add_u32 s6, s10, s6
	s_addc_u32 s7, s11, 0
	v_mov_b32_e32 v137, 0
	v_mov_b32_e32 v138, 0
	v_mov_b32_e32 v139, 0
	v_mov_b32_e32 v140, 0
	v_mov_b32_e32 v141, 0
	s_and_saveexec_b64 s[12:13], vcc
	s_cbranch_execz .LBB15_18
	v_ashrrev_i32_e32 v153, 31, v152
	v_lshl_add_u64 v[134:135], v[152:153], 4, s[6:7]
	global_load_dwordx4 v[138:141], v[134:135], off

.LBB15_21:
	s_mul_i32 s6, s23, 0x222
	v_subrev_u32_e32 v153, s6, v170
	v_mfma_f32_32x32x16_f16 v[66:81], v[250:253], v[194:197], v[66:81]
	s_and_b32 s7, s19, 1
	s_mulk_i32 s7, 0x6000
	v_mfma_f32_32x32x16_f16 v[2:17], v[174:177], v[238:241], v[2:17]
	v_lshrrev_b32_e32 v173, 2, v153
	s_and_b32 s6, s23, 1
	v_mfma_f32_32x32x16_f16 v[34:49], v[174:177], v[242:245], v[34:49]
	s_mul_i32 s23, s23, 0xffff7780
	s_add_i32 s7, s7, 0x13700
	v_mfma_f32_32x32x16_f16 v[34:49], v[250:253], v[238:241], v[34:49]
	v_bitop3_b32 v174, v173, v159, 3 bitop3:0x6c
	v_add_u32_e32 v234, s18, v171
	v_bitop3_b32 v173, v173, v160, 3 bitop3:0x6c
	s_mul_i32 s6, s6, 0x9b80
	v_add_u32_e32 v154, s23, v172
	v_lshl_or_b32 v155, v169, 4, s7
	v_lshl_add_u32 v174, v174, 4, v234
	v_lshl_add_u32 v173, v173, 4, v234
	v_add3_u32 v182, v174, s6, v154
	v_add3_u32 v173, v173, s6, v154
	v_add_u32_e32 v155, v155, v168
	ds_read_b128 v[174:177], v182
	ds_read_b128 v[178:181], v173
	ds_read_b128 v[182:185], v182 offset:2048
	ds_read_b128 v[186:189], v173 offset:2048
	ds_read_b128 v[190:193], v155
	v_lshl_or_b32 v173, v165, 4, s7
	v_add_u32_e32 v173, v173, v168
	ds_read_b128 v[194:197], v173
	s_waitcnt lgkmcnt(1)
	v_mfma_f32_32x32x16_f16 v[82:97], v[190:193], v[174:177], v[82:97]
	ds_read_b128 v[198:201], v155 offset:2048
	ds_read_b128 v[202:205], v173 offset:2048
	v_add_u32_e32 v206, 1, v153
	v_lshrrev_b32_e32 v210, 2, v206
	v_bitop3_b32 v206, v210, v159, 3 bitop3:0x6c
	v_bitop3_b32 v210, v210, v160, 3 bitop3:0x6c
	v_lshl_add_u32 v206, v206, 4, v234
	v_mfma_f32_32x32x16_f16 v[114:129], v[190:193], v[178:181], v[114:129]
	v_lshl_add_u32 v210, v210, 4, v234
	v_add3_u32 v214, v206, s6, v154
	v_add3_u32 v218, v210, s6, v154
	ds_read_b128 v[206:209], v214 offset:64
	ds_read_b128 v[210:213], v218 offset:64
	v_add_u32_e32 v153, 2, v153
	v_lshrrev_b32_e32 v153, 2, v153
	s_waitcnt lgkmcnt(4)
	v_mfma_f32_32x32x16_f16 v[114:129], v[194:197], v[174:177], v[114:129]
	ds_read_b128 v[214:217], v214 offset:2112
	ds_read_b128 v[218:221], v218 offset:2112
	s_add_i32 s19, s19, 1
	v_mfma_f32_32x32x16_f16 v[50:65], v[190:193], v[182:185], v[50:65]
	ds_read_b128 v[222:225], v155 offset:8192
	ds_read_b128 v[226:229], v173 offset:8192
	v_mfma_f32_32x32x16_f16 v[98:113], v[190:193], v[186:189], v[98:113]
	ds_read_b128 v[190:193], v155 offset:10240
	ds_read_b128 v[230:233], v173 offset:10240
	v_mfma_f32_32x32x16_f16 v[98:113], v[194:197], v[182:185], v[98:113]
	v_bitop3_b32 v194, v153, v159, 3 bitop3:0x6c
	v_bitop3_b32 v153, v153, v160, 3 bitop3:0x6c
	v_lshl_add_u32 v194, v194, 4, v234
	v_lshl_add_u32 v153, v153, 4, v234
	v_add3_u32 v238, v194, s6, v154
	v_add3_u32 v153, v153, s6, v154
	ds_read_b128 v[194:197], v238 offset:128
	ds_read_b128 v[234:237], v153 offset:128
	s_waitcnt lgkmcnt(11)
	v_mfma_f32_32x32x16_f16 v[18:33], v[198:201], v[174:177], v[18:33]
	ds_read_b128 v[238:241], v238 offset:2176
	ds_read_b128 v[242:245], v153 offset:2176
	s_and_b32 s6, s19, 1
	s_mul_i32 s12, s6, 0x6000
	s_add_i32 s12, s12, 0x13700
	v_lshl_add_u32 v153, v162, 4, s12
	v_mfma_f32_32x32x16_f16 v[66:81], v[198:201], v[178:181], v[66:81]
	ds_read_b128 v[178:181], v155 offset:16384
	ds_read_b128 v[246:249], v173 offset:16384
	s_waitcnt lgkmcnt(14)
	v_mfma_f32_32x32x16_f16 v[66:81], v[202:205], v[174:177], v[66:81]
	ds_read_b128 v[174:177], v155 offset:18432
	ds_read_b128 v[250:253], v173 offset:18432
	v_mfma_f32_32x32x16_f16 v[2:17], v[198:201], v[182:185], v[2:17]
	v_mfma_f32_32x32x16_f16 v[34:49], v[198:201], v[186:189], v[34:49]
	v_mfma_f32_32x32x16_f16 v[34:49], v[202:205], v[182:185], v[34:49]
	s_waitcnt lgkmcnt(11)
	v_mfma_f32_32x32x16_f16 v[82:97], v[222:225], v[206:209], v[82:97]
	v_mfma_f32_32x32x16_f16 v[114:129], v[222:225], v[210:213], v[114:129]
	s_waitcnt lgkmcnt(10)
	v_mfma_f32_32x32x16_f16 v[114:129], v[226:229], v[206:209], v[114:129]
	v_mfma_f32_32x32x16_f16 v[50:65], v[222:225], v[214:217], v[50:65]
	v_mfma_f32_32x32x16_f16 v[98:113], v[222:225], v[218:221], v[98:113]
	v_mfma_f32_32x32x16_f16 v[98:113], v[226:229], v[214:217], v[98:113]
	s_waitcnt lgkmcnt(9)
	v_mfma_f32_32x32x16_f16 v[18:33], v[190:193], v[206:209], v[18:33]
	v_mfma_f32_32x32x16_f16 v[66:81], v[190:193], v[210:213], v[66:81]
	s_waitcnt lgkmcnt(8)
	v_mfma_f32_32x32x16_f16 v[66:81], v[230:233], v[206:209], v[66:81]
	v_mfma_f32_32x32x16_f16 v[2:17], v[190:193], v[214:217], v[2:17]
	v_mfma_f32_32x32x16_f16 v[34:49], v[190:193], v[218:221], v[34:49]
	v_mfma_f32_32x32x16_f16 v[34:49], v[230:233], v[214:217], v[34:49]
	s_waitcnt vmcnt(0)
	s_andn2_b64 vcc, exec, s[4:5]
	s_cbranch_vccnz .LBB15_12
	s_and_b32 s6, s22, 1
	s_mul_i32 s6, s6, 0x9b80
	v_cmp_gt_i32_e32 vcc, s21, v152
	v_lshrrev_b32_e32 v130, 4, v152
	s_and_saveexec_b64 s[4:5], vcc
	v_bitop3_b32 v131, v130, v152, 3 bitop3:0x6c
	v_lshl_add_u32 v131, v131, 4, s6
	ds_write_b128 v131, v[138:141]
	s_or_b64 exec, exec, s[4:5]
	v_add_u32_e32 v131, s20, v0
	v_cmp_gt_i32_e32 vcc, s21, v131
	s_and_saveexec_b64 s[4:5], vcc
	s_cbranch_execz .LBB15_11
	v_bitop3_b32 v130, v130, v131, 3 bitop3:0x6c
	v_lshl_add_u32 v130, v130, 4, s6
	ds_write_b128 v130, v[134:137]
	s_branch .LBB15_11

	.amdhsa_kernel _Z11conv_kernelILi8ELi128ELi0EEvPK15HIP_vector_typeIjLj4EES3_PKfS5_S5_PDF16_PfS7_
		.amdhsa_group_segment_fixed_size 130304
		.amdhsa_private_segment_fixed_size 0
		.amdhsa_kernarg_size 64
		.amdhsa_user_sgpr_count 2
		.amdhsa_user_sgpr_dispatch_ptr 0
		.amdhsa_user_sgpr_queue_ptr 0
		.amdhsa_user_sgpr_kernarg_segment_ptr 1
		.amdhsa_user_sgpr_dispatch_id 0
		.amdhsa_user_sgpr_kernarg_preload_length 0
		.amdhsa_user_sgpr_kernarg_preload_offset 0
		.amdhsa_user_sgpr_private_segment_size 0
		.amdhsa_uses_dynamic_stack 0
		.amdhsa_enable_private_segment 0
		.amdhsa_system_sgpr_workgroup_id_x 1
		.amdhsa_system_sgpr_workgroup_id_y 1
		.amdhsa_system_sgpr_workgroup_id_z 0
		.amdhsa_system_sgpr_workgroup_info 0
		.amdhsa_system_vgpr_workitem_id 0
		.amdhsa_next_free_vgpr 256
		.amdhsa_next_free_sgpr 96
		.amdhsa_accum_offset 256
		.amdhsa_reserve_vcc 1
		.amdhsa_float_round_mode_32 0
		.amdhsa_float_round_mode_16_64 0
		.amdhsa_float_denorm_mode_32 3
		.amdhsa_float_denorm_mode_16_64 3
		.amdhsa_dx10_clamp 1
		.amdhsa_ieee_mode 1
		.amdhsa_fp16_overflow 0
		.amdhsa_tg_split 0
		.amdhsa_exception_fp_ieee_invalid_op 0
		.amdhsa_exception_fp_denorm_src 0
		.amdhsa_exception_fp_ieee_div_zero 0
		.amdhsa_exception_fp_ieee_overflow 0
		.amdhsa_exception_fp_ieee_underflow 0
		.amdhsa_exception_fp_ieee_inexact 0
		.amdhsa_exception_int_div_zero 0
	.end_amdhsa_kernel

amdhsa.kernels:
  - .agpr_count:     0
    .args:
      - .actual_access:  read_only
        .address_space:  global
        .offset:         0
        .size:           8
        .value_kind:     global_buffer
      - .actual_access:  write_only
        .address_space:  global
        .offset:         8
        .size:           8
        .value_kind:     global_buffer
    .group_segment_fixed_size: 0
    .kernarg_segment_align: 8
    .kernarg_segment_size: 16
    .language:       OpenCL C
    .language_version:
      - 2
      - 0
    .max_flat_workgroup_size: 256
    .name:           _Z13prep_x_kernelPKfP15HIP_vector_typeIjLj4EE
    .private_segment_fixed_size: 0
    .sgpr_count:     23
    .sgpr_spill_count: 0
    .symbol:         _Z13prep_x_kernelPKfP15HIP_vector_typeIjLj4EE.kd
    .uniform_work_group_size: 1
    .uses_dynamic_stack: false
    .vgpr_count:     36
    .vgpr_spill_count: 0
    .wavefront_size: 64
  - .agpr_count:     0
    .args:
      - .actual_access:  read_only
        .address_space:  global
        .offset:         0
        .size:           8
        .value_kind:     global_buffer
      - .actual_access:  write_only
        .address_space:  global
        .offset:         8
        .size:           8
        .value_kind:     global_buffer
      - .offset:         16
        .size:           4
        .value_kind:     by_value
      - .offset:         20
        .size:           4
        .value_kind:     by_value
      - .offset:         24
        .size:           4
        .value_kind:     by_value
      - .offset:         28
        .size:           4
        .value_kind:     by_value
    .group_segment_fixed_size: 0
    .kernarg_segment_align: 8
    .kernarg_segment_size: 32
    .language:       OpenCL C
    .language_version:
      - 2
      - 0
    .max_flat_workgroup_size: 256
    .name:           _Z13prep_w_kernelPKfP15HIP_vector_typeIjLj4EEiiii
    .private_segment_fixed_size: 0
    .sgpr_count:     15
    .sgpr_spill_count: 0
    .symbol:         _Z13prep_w_kernelPKfP15HIP_vector_typeIjLj4EEiiii.kd
    .uniform_work_group_size: 1
    .uses_dynamic_stack: false
    .vgpr_count:     34
    .vgpr_spill_count: 0
    .wavefront_size: 64
  - .agpr_count:     0
    .args:
      - .actual_access:  write_only
        .address_space:  global
        .offset:         0
        .size:           8
        .value_kind:     global_buffer
    .group_segment_fixed_size: 0
    .kernarg_segment_align: 8
    .kernarg_segment_size: 8
    .language:       OpenCL C
    .language_version:
      - 2
      - 0
    .max_flat_workgroup_size: 256
    .name:           _Z18zero_border_kernelP15HIP_vector_typeIjLj4EE
    .private_segment_fixed_size: 0
    .sgpr_count:     12
    .sgpr_spill_count: 0
    .symbol:         _Z18zero_border_kernelP15HIP_vector_typeIjLj4EE.kd
    .uniform_work_group_size: 1
    .uses_dynamic_stack: false
    .vgpr_count:     6
    .vgpr_spill_count: 0
    .wavefront_size: 64
  - .agpr_count:     0
    .args:
      - .actual_access:  read_only
        .address_space:  global
        .offset:         0
        .size:           8
        .value_kind:     global_buffer
      - .address_space:  global
        .offset:         8
        .size:           8
        .value_kind:     global_buffer
      - .actual_access:  read_only
        .address_space:  global
        .offset:         16
        .size:           8
        .value_kind:     global_buffer
      - .actual_access:  read_only
        .address_space:  global
        .offset:         24
        .size:           8
        .value_kind:     global_buffer
      - .actual_access:  read_only
        .address_space:  global
        .offset:         32
        .size:           8
        .value_kind:     global_buffer
      - .actual_access:  write_only
        .address_space:  global
        .offset:         40
        .size:           8
        .value_kind:     global_buffer
    .group_segment_fixed_size: 154880
    .kernarg_segment_align: 8
    .kernarg_segment_size: 48
    .language:       OpenCL C
    .language_version:
      - 2
      - 0
    .max_flat_workgroup_size: 512
    .name:           _Z12conv1_kernelPKfPK15HIP_vector_typeIjLj4EES0_S0_S0_PDF16_
    .private_segment_fixed_size: 0
    .sgpr_count:     46
    .sgpr_spill_count: 0
    .symbol:         _Z12conv1_kernelPKfPK15HIP_vector_typeIjLj4EES0_S0_S0_PDF16_.kd
    .uniform_work_group_size: 1
    .uses_dynamic_stack: false
    .vgpr_count:     256
    .vgpr_spill_count: 0
    .wavefront_size: 64
  - .agpr_count:     0
    .args:
      - .actual_access:  read_only
        .address_space:  global
        .offset:         0
        .size:           8
        .value_kind:     global_buffer
      - .actual_access:  read_only
        .address_space:  global
        .offset:         8
        .size:           8
        .value_kind:     global_buffer
      - .actual_access:  read_only
        .address_space:  global
        .offset:         16
        .size:           8
        .value_kind:     global_buffer
      - .actual_access:  write_only
        .address_space:  global
        .offset:         24
        .size:           8
        .value_kind:     global_buffer
      - .actual_access:  write_only
        .address_space:  global
        .offset:         32
        .size:           8
        .value_kind:     global_buffer
    .group_segment_fixed_size: 116480
    .kernarg_segment_align: 8
    .kernarg_segment_size: 40
    .language:       OpenCL C
    .language_version:
      - 2
      - 0
    .max_flat_workgroup_size: 512
    .name:           _Z12conv3_kernelPK15HIP_vector_typeIjLj4EES2_PKfPfS5_
    .private_segment_fixed_size: 0
    .sgpr_count:     22
    .sgpr_spill_count: 0
    .symbol:         _Z12conv3_kernelPK15HIP_vector_typeIjLj4EES2_PKfPfS5_.kd
    .uniform_work_group_size: 1
    .uses_dynamic_stack: false
    .vgpr_count:     122
    .vgpr_spill_count: 0
    .wavefront_size: 64
  - .agpr_count:     0
    .args:
      - .actual_access:  read_only
        .address_space:  global
        .offset:         0
        .size:           8
        .value_kind:     global_buffer
      - .actual_access:  read_only
        .address_space:  global
        .offset:         8
        .size:           8
        .value_kind:     global_buffer
      - .actual_access:  write_only
        .address_space:  global
        .offset:         16
        .size:           8
        .value_kind:     global_buffer
      - .address_space:  global
        .offset:         24
        .size:           8
        .value_kind:     global_buffer
    .group_segment_fixed_size: 32768
    .kernarg_segment_align: 8
    .kernarg_segment_size: 32
    .language:       OpenCL C
    .language_version:
      - 2
      - 0
    .max_flat_workgroup_size: 256
    .name:           _Z15nms_hist_kernelPKfS0_PjS1_
    .private_segment_fixed_size: 0
    .sgpr_count:     102
    .sgpr_spill_count: 0
    .symbol:         _Z15nms_hist_kernelPKfS0_PjS1_.kd
    .uniform_work_group_size: 1
    .uses_dynamic_stack: false
    .vgpr_count:     128
    .vgpr_spill_count: 0
    .wavefront_size: 64
  - .agpr_count:     0
    .args:
      - .actual_access:  read_only
        .address_space:  global
        .offset:         0
        .size:           8
        .value_kind:     global_buffer
      - .actual_access:  write_only
        .address_space:  global
        .offset:         8
        .size:           8
        .value_kind:     global_buffer
    .group_segment_fixed_size: 4096
    .kernarg_segment_align: 8
    .kernarg_segment_size: 16
    .language:       OpenCL C
    .language_version:
      - 2
      - 0
    .max_flat_workgroup_size: 1024
    .name:           _Z17select_bin_kernelPKjPi
    .private_segment_fixed_size: 0
    .sgpr_count:     23
    .sgpr_spill_count: 0
    .symbol:         _Z17select_bin_kernelPKjPi.kd
    .uniform_work_group_size: 1
    .uses_dynamic_stack: false
    .vgpr_count:     13
    .vgpr_spill_count: 0
    .wavefront_size: 64
  - .agpr_count:     0
    .args:
      - .actual_access:  read_only
        .address_space:  global
        .offset:         0
        .size:           8
        .value_kind:     global_buffer
      - .actual_access:  read_only
        .address_space:  global
        .offset:         8
        .size:           8
        .value_kind:     global_buffer
      - .address_space:  global
        .offset:         16
        .size:           8
        .value_kind:     global_buffer
      - .actual_access:  write_only
        .address_space:  global
        .offset:         24
        .size:           8
        .value_kind:     global_buffer
    .group_segment_fixed_size: 2052
    .kernarg_segment_align: 8
    .kernarg_segment_size: 32
    .language:       OpenCL C
    .language_version:
      - 2
      - 0
    .max_flat_workgroup_size: 512
    .name:           _Z14collect_kernelPKjS0_PiS1_
    .private_segment_fixed_size: 0
    .sgpr_count:     70
    .sgpr_spill_count: 0
    .symbol:         _Z14collect_kernelPKjS0_PiS1_.kd
    .uniform_work_group_size: 1
    .uses_dynamic_stack: false
    .vgpr_count:     34
    .vgpr_spill_count: 0
    .wavefront_size: 64
  - .agpr_count:     0
    .args:
      - .actual_access:  read_only
        .address_space:  global
        .offset:         0
        .size:           8
        .value_kind:     global_buffer
      - .actual_access:  read_only
        .address_space:  global
        .offset:         8
        .size:           8
        .value_kind:     global_buffer
      - .actual_access:  read_only
        .address_space:  global
        .offset:         16
        .size:           8
        .value_kind:     global_buffer
      - .actual_access:  read_only
        .address_space:  global
        .offset:         24
        .size:           8
        .value_kind:     global_buffer
      - .actual_access:  write_only
        .address_space:  global
        .offset:         32
        .size:           8
        .value_kind:     global_buffer
    .group_segment_fixed_size: 49664
    .kernarg_segment_align: 8
    .kernarg_segment_size: 40
    .language:       OpenCL C
    .language_version:
      - 2
      - 0
    .max_flat_workgroup_size: 1024
    .name:           _Z11rank_kernelPKfS0_PKiS2_Pi
    .private_segment_fixed_size: 0
    .sgpr_count:     23
    .sgpr_spill_count: 0
    .symbol:         _Z11rank_kernelPKfS0_PKiS2_Pi.kd
    .uniform_work_group_size: 1
    .uses_dynamic_stack: false
    .vgpr_count:     12
    .vgpr_spill_count: 0
    .wavefront_size: 64
  - .agpr_count:     0
    .args:
      - .actual_access:  read_only
        .address_space:  global
        .offset:         0
        .size:           8
        .value_kind:     global_buffer
      - .actual_access:  read_only
        .address_space:  global
        .offset:         8
        .size:           8
        .value_kind:     global_buffer
      - .actual_access:  write_only
        .address_space:  global
        .offset:         16
        .size:           8
        .value_kind:     global_buffer
      - .actual_access:  write_only
        .address_space:  global
        .offset:         24
        .size:           8
        .value_kind:     global_buffer
    .group_segment_fixed_size: 0
    .kernarg_segment_align: 8
    .kernarg_segment_size: 32
    .language:       OpenCL C
    .language_version:
      - 2
      - 0
    .max_flat_workgroup_size: 256
    .name:           _Z15prep_kvw_kernelPKfS0_PDF16_S1_
    .private_segment_fixed_size: 0
    .sgpr_count:     14
    .sgpr_spill_count: 0
    .symbol:         _Z15prep_kvw_kernelPKfS0_PDF16_S1_.kd
    .uniform_work_group_size: 1
    .uses_dynamic_stack: false
    .vgpr_count:     7
    .vgpr_spill_count: 0
    .wavefront_size: 64
  - .agpr_count:     0
    .args:
      - .actual_access:  read_only
        .address_space:  global
        .offset:         0
        .size:           8
        .value_kind:     global_buffer
      - .actual_access:  read_only
        .address_space:  global
        .offset:         8
        .size:           8
        .value_kind:     global_buffer
      - .actual_access:  read_only
        .address_space:  global
        .offset:         16
        .size:           8
        .value_kind:     global_buffer
      - .actual_access:  read_only
        .address_space:  global
        .offset:         24
        .size:           8
        .value_kind:     global_buffer
      - .actual_access:  write_only
        .address_space:  global
        .offset:         32
        .size:           8
        .value_kind:     global_buffer
    .group_segment_fixed_size: 67856
    .kernarg_segment_align: 8
    .kernarg_segment_size: 40
    .language:       OpenCL C
    .language_version:
      - 2
      - 0
    .max_flat_workgroup_size: 448
    .name:           _Z17cross_attn_kernelPKDF16_S0_S0_S0_Pf
    .private_segment_fixed_size: 0
    .sgpr_count:     26
    .sgpr_spill_count: 0
    .symbol:         _Z17cross_attn_kernelPKDF16_S0_S0_S0_Pf.kd
    .uniform_work_group_size: 1
    .uses_dynamic_stack: false
    .vgpr_count:     74
    .vgpr_spill_count: 0
    .wavefront_size: 64
  - .agpr_count:     0
    .args:
      - .offset:         0
        .size:           424
        .value_kind:     by_value
      - .offset:         424
        .size:           88
        .value_kind:     by_value
    .group_segment_fixed_size: 137216
    .kernarg_segment_align: 8
    .kernarg_segment_size: 512
    .language:       OpenCL C
    .language_version:
      - 2
      - 0
    .max_flat_workgroup_size: 512
    .name:           _Z12tailA_kernel5TailP3KvP
    .private_segment_fixed_size: 0
    .sgpr_count:     44
    .sgpr_spill_count: 0
    .symbol:         _Z12tailA_kernel5TailP3KvP.kd
    .uniform_work_group_size: 1
    .uses_dynamic_stack: false
    .vgpr_count:     200
    .vgpr_spill_count: 0
    .wavefront_size: 64
  - .agpr_count:     0
    .args:
      - .offset:         0
        .size:           424
        .value_kind:     by_value
      - .offset:         424
        .size:           88
        .value_kind:     by_value
    .group_segment_fixed_size: 146592
    .kernarg_segment_align: 8
    .kernarg_segment_size: 512
    .language:       OpenCL C
    .language_version:
      - 2
      - 0
    .max_flat_workgroup_size: 512
    .name:           _Z12tailB_kernel5TailP3KvP
    .private_segment_fixed_size: 0
    .sgpr_count:     44
    .sgpr_spill_count: 0
    .symbol:         _Z12tailB_kernel5TailP3KvP.kd
    .uniform_work_group_size: 1
    .uses_dynamic_stack: false
    .vgpr_count:     216
    .vgpr_spill_count: 0
    .wavefront_size: 64
  - .agpr_count:     0
    .args:
      - .offset:         0
        .size:           424
        .value_kind:     by_value
    .group_segment_fixed_size: 36896
    .kernarg_segment_align: 8
    .kernarg_segment_size: 424
    .language:       OpenCL C
    .language_version:
      - 2
      - 0
    .max_flat_workgroup_size: 512
    .name:           _Z12tailC_kernel5TailP
    .private_segment_fixed_size: 0
    .sgpr_count:     58
    .sgpr_spill_count: 0
    .symbol:         _Z12tailC_kernel5TailP.kd
    .uniform_work_group_size: 1
    .uses_dynamic_stack: false
    .vgpr_count:     113
    .vgpr_spill_count: 0
    .wavefront_size: 64
  - .agpr_count:     0
    .args:
      - .offset:         0
        .size:           344
        .value_kind:     by_value
    .group_segment_fixed_size: 0
    .kernarg_segment_align: 8
    .kernarg_segment_size: 344
    .language:       OpenCL C
    .language_version:
      - 2
      - 0
    .max_flat_workgroup_size: 256
    .name:           _Z15prep_all_kernel5PrepP
    .private_segment_fixed_size: 0
    .sgpr_count:     31
    .sgpr_spill_count: 0
    .symbol:         _Z15prep_all_kernel5PrepP.kd
    .uniform_work_group_size: 1
    .uses_dynamic_stack: false
    .vgpr_count:     39
    .vgpr_spill_count: 0
    .wavefront_size: 64
  - .agpr_count:     0
    .args:
      - .actual_access:  read_only
        .address_space:  global
        .offset:         0
        .size:           8
        .value_kind:     global_buffer
      - .actual_access:  read_only
        .address_space:  global
        .offset:         8
        .size:           8
        .value_kind:     global_buffer
      - .actual_access:  read_only
        .address_space:  global
        .offset:         16
        .size:           8
        .value_kind:     global_buffer
      - .actual_access:  read_only
        .address_space:  global
        .offset:         24
        .size:           8
        .value_kind:     global_buffer
      - .actual_access:  read_only
        .address_space:  global
        .offset:         32
        .size:           8
        .value_kind:     global_buffer
      - .actual_access:  write_only
        .address_space:  global
        .offset:         40
        .size:           8
        .value_kind:     global_buffer
      - .actual_access:  read_only
        .address_space:  global
        .offset:         48
        .size:           8
        .value_kind:     global_buffer
      - .actual_access:  read_only
        .address_space:  global
        .offset:         56
        .size:           8
        .value_kind:     global_buffer
    .group_segment_fixed_size: 130304
    .kernarg_segment_align: 8
    .kernarg_segment_size: 64
    .language:       OpenCL C
    .language_version:
      - 2
      - 0
    .max_flat_workgroup_size: 512
    .name:           _Z11conv_kernelILi8ELi128ELi0EEvPK15HIP_vector_typeIjLj4EES3_PKfS5_S5_PDF16_PfS7_
    .private_segment_fixed_size: 0
    .sgpr_count:     30
    .sgpr_spill_count: 0
    .symbol:         _Z11conv_kernelILi8ELi128ELi0EEvPK15HIP_vector_typeIjLj4EES3_PKfS5_S5_PDF16_PfS7_.kd
    .uniform_work_group_size: 1
    .uses_dynamic_stack: false
    .vgpr_count:     256
    .vgpr_spill_count: 0
    .wavefront_size: 64
